# nt hints plus MoE expert 3-5 weight conversion moved out of the prologue into 64 workgroups running beside the first GEMM phase (192 workgroups do the GEMM)
# speedup vs baseline: 1.0162x; 1.0099x over previous
_Z10hybrid_fwd4Args:
	s_load_dwordx8 s[52:59], s[0:1], 0x100
	s_load_dwordx2 s[76:77], s[0:1], 0x120
	s_mov_b32 s96, s2
	v_cmp_gt_u32_e64 s[4:5], 64, v0
	s_and_saveexec_b64 s[2:3], s[4:5]
	v_lshl_add_u32 v1, v0, 2, 0
	v_add_u32_e32 v1, 0x26000, v1
	v_mov_b32_e32 v2, 0
	ds_write_b32 v1, v2
	s_or_b64 exec, exec, s[2:3]
	s_load_dwordx16 s[8:23], s[0:1], 0x40
	s_load_dwordx16 s[80:95], s[0:1], 0xc0
	s_waitcnt lgkmcnt(0)
	s_mov_b32 s98, 0
	s_mov_b32 s99, 0
	s_mov_b32 s100, 3
	s_barrier
	v_writelane_b32 v239, s8, 0
	s_getreg_b32 s2, hwreg(HW_REG_XCC_ID, 0, 4)
	s_and_b32 s78, s2, 15
	v_writelane_b32 v239, s9, 1
	v_writelane_b32 v239, s10, 2
	v_writelane_b32 v239, s11, 3
	v_writelane_b32 v239, s12, 4
	v_writelane_b32 v239, s13, 5
	v_writelane_b32 v239, s14, 6
	v_writelane_b32 v239, s15, 7
	v_writelane_b32 v239, s16, 8
	v_writelane_b32 v239, s17, 9
	v_writelane_b32 v239, s18, 10
	v_writelane_b32 v239, s19, 11
	v_writelane_b32 v239, s20, 12
	v_writelane_b32 v239, s21, 13
	v_writelane_b32 v239, s22, 14
	v_writelane_b32 v239, s23, 15
	v_cmp_eq_u32_e64 s[6:7], 0, v0
	s_mov_b64 s[2:3], exec
	s_nop 0
	v_writelane_b32 v239, s6, 16
	s_nop 1
	v_writelane_b32 v239, s7, 17
	s_and_b64 s[6:7], s[2:3], s[6:7]
	s_mov_b64 exec, s[6:7]
	s_cbranch_execz .LBB0_5
	s_mov_b64 s[6:7], exec
	v_mbcnt_lo_u32_b32 v1, s6, 0
	v_mbcnt_hi_u32_b32 v1, s7, v1
	v_cmp_eq_u32_e32 vcc, 0, v1
	s_and_b64 s[8:9], exec, vcc
	s_mov_b64 exec, s[8:9]
	s_cbranch_execz .LBB0_5
	s_lshl_b32 s8, s78, 8
	s_bcnt1_i32_b64 s6, s[6:7]
	v_mov_b32_e32 v1, s8
	v_mov_b32_e32 v2, s6
	global_atomic_add v1, v2, s[58:59] offset:1024

.Lconv_entry:
	s_movk_i32 s0, 0x4200
	v_lshl_or_b32 v69, s96, 3, v186
	v_mad_u32_u24 v31, v186, s0, 0
	s_movk_i32 s0, 0xe00
	v_and_b32_e32 v1, 7, v0
	v_cmp_gt_i32_e32 vcc, s0, v69
	v_bfe_u32 v66, v0, 3, 3
	v_mov_b32_e32 v3, 0
	v_lshlrev_b32_e32 v2, 4, v1
	s_movk_i32 s0, 0x840
	s_lshl_b32 s20, s96, 10
	v_lshlrev_b32_e32 v78, 2, v1
	v_add_u32_e32 v79, v31, v2
	v_mul_u32_u24_e32 v4, 0x84, v66
	v_mad_u32_u24 v1, v1, s0, v31
	v_lshl_add_u64 v[80:81], s[58:59], 0, v[2:3]
	s_mov_b64 s[0:1], 0x100000
	v_lshl_or_b32 v74, v186, 7, s20
	s_waitcnt lgkmcnt(0)
	s_lshl_b32 s3, s2, 3
	s_mov_b32 s9, 0
	v_lshl_add_u64 v[18:19], v[80:81], 0, s[0:1]
	v_lshl_add_u32 v75, v66, 2, v1
	s_mov_b64 s[0:1], 0x1c100000
	v_or_b32_e32 v1, v74, v66
	s_movk_i32 s21, 0x1c00
	v_add_u32_e32 v40, v79, v4
	v_or_b32_e32 v68, 8, v66
	v_or_b32_e32 v70, 16, v66
	v_or_b32_e32 v72, 24, v66
	v_lshl_add_u64 v[20:21], v[80:81], 0, s[0:1]
	v_lshl_add_u64 v[22:23], s[90:91], 0, v[2:3]
	v_lshl_add_u64 v[24:25], s[92:93], 0, v[2:3]
	v_lshl_add_u64 v[26:27], s[94:95], 0, v[2:3]
	v_mul_lo_u32 v1, v1, s21
	s_mov_b32 s22, 0xe0000
	s_mul_i32 s23, s3, 0xe0000
	s_movk_i32 s24, 0x60
	s_mov_b32 s25, 0xff200000
	s_mov_b32 s26, 0x38000
	s_mov_b32 s27, 0x70000
	s_mov_b32 s28, 0xa8000
	s_mov_b32 s29, 0x118000
	s_mov_b32 s30, 0x150000
	s_mov_b32 s31, 0x188000
	s_mov_b32 s33, 0x1c0000
	s_mov_b32 s34, 0x1f8000
	s_mov_b32 s35, 0x230000
	s_mov_b32 s60, 0x268000
	s_mov_b32 s61, 0x2a0000
	s_mov_b32 s62, 0x2d8000
	s_mov_b32 s63, 0x310000
	s_mov_b32 s64, 0x348000
	v_add_u32_e32 v41, 0x420, v40
	v_add_u32_e32 v42, 0x428, v40
	v_add_u32_e32 v43, 0x840, v40
	v_add_u32_e32 v44, 0x848, v40
	v_add_u32_e32 v45, 0xc60, v40
	v_add_u32_e32 v46, 0xc68, v40
	v_add_u32_e32 v47, 0x1080, v40
	v_add_u32_e32 v48, 0x1088, v40
	v_add_u32_e32 v49, 0x14a0, v40
	v_add_u32_e32 v50, 0x14a8, v40
	v_add_u32_e32 v51, 0x18c0, v40
	v_add_u32_e32 v52, 0x18c8, v40
	v_add_u32_e32 v53, 0x1ce0, v40
	v_add_u32_e32 v54, 0x1ce8, v40
	v_add_u32_e32 v55, 0x2100, v40
	v_add_u32_e32 v56, 0x2108, v40
	v_add_u32_e32 v57, 0x2520, v40
	s_mov_b32 s65, 0xc3e00000
	s_movk_i32 s66, 0xdff
	v_add_u32_e32 v58, 0x2528, v40
	v_add_u32_e32 v59, 0x2940, v40
	v_add_u32_e32 v60, 0x2948, v40
	v_add_u32_e32 v61, 0x2d60, v40
	v_add_u32_e32 v62, 0x2d68, v40
	v_add_u32_e32 v63, 0x3180, v40
	v_add_u32_e32 v64, 0x3188, v40
	v_mov_b32_e32 v65, 0x43e00000
	v_mov_b32_e32 v67, 0x3800000
	s_mov_b32 s8, s98
	s_branch .LBB0_8
.LBB0_7:
	s_or_b64 exec, exec, s[12:13]
	s_add_i32 s8, s8, 1
	s_cmp_lg_u32 s8, s100
	s_cbranch_scc0 .LBB0_15

.LBB0_15:
	s_cmp_eq_u32 s99, 0
	s_cbranch_scc0 .Lconv_ret_h0
	v_lshlrev_b32_e32 v67, 2, v0
	v_and_b32_e32 v71, 60, v67
	v_bfe_u32 v93, v0, 4, 2
	v_lshlrev_b32_e32 v1, 2, v71
	v_mul_u32_u24_e32 v2, 0x104, v93
	v_add3_u32 v73, v31, v1, v2
	v_lshlrev_b32_e32 v1, 3, v0
	v_and_b32_e32 v2, 56, v1
	v_mul_u32_u24_e32 v3, 0x104, v2
	v_lshlrev_b32_e32 v4, 2, v66
	s_movk_i32 s0, 0x400
	v_mov_b32_e32 v77, 0
	v_add3_u32 v88, v31, v3, v4
	v_or_b32_e32 v89, 32, v66
	v_or_b32_e32 v90, 40, v66
	v_or_b32_e32 v91, 48, v66
	v_or_b32_e32 v92, 56, v66
	v_cmp_gt_i32_e64 s[6:7], s0, v69
	v_lshlrev_b32_e32 v76, 1, v2
	v_lshlrev_b32_e32 v94, 6, v186
	s_and_saveexec_b64 s[0:1], s[6:7]
	s_cbranch_execz .LBB0_50
	v_lshl_add_u64 v[2:3], s[58:59], 0, v[76:77]
	s_mov_b64 s[8:9], 0x3da00000
	v_lshl_add_u64 v[82:83], v[2:3], 0, s[8:9]
	v_lshl_or_b32 v77, s96, 9, v94
	s_lshl_b32 s14, s3, 6
	s_mov_b64 s[8:9], 0
	s_movk_i32 s15, 0x800
	s_movk_i32 s16, 0x3ff
	v_mov_b32_e32 v95, v69
	s_branch .LBB0_18

.LBB0_400:
	s_cmp_lt_i32 s76, 2
	s_cselect_b64 s[6:7], -1, 0
	s_add_u32 s82, s58, 0x32100000
	s_addc_u32 s83, s59, 0
	s_and_b64 s[0:1], s[6:7], s[0:1]
	s_andn2_b64 vcc, exec, s[0:1]
	s_cbranch_vccnz .LBB0_417
	s_mov_b32 s101, s2
	s_cmpk_lt_i32 s96, 192
	s_cbranch_scc1 .Lh0_gemm
	s_sub_i32 s96, s96, 192
	s_movk_i32 s2, 64
	s_mov_b32 s98, 3
	s_mov_b32 s100, 6
	s_mov_b32 s99, 1
	s_branch .Lconv_entry
.Lconv_ret_h0:
	s_mov_b32 s99, 0
	s_add_i32 s96, s96, 192
	s_mov_b32 s2, s101
	s_mov_b64 exec, -1
	s_mov_b64 s[0:1], -1
	s_branch .LBB0_417
.Lh0_gemm:
	s_movk_i32 s2, 192
	s_cmpk_gt_i32 s96, 0x5ff
	v_readfirstlane_b32 s7, v0
	s_cbranch_scc1 .LBB0_417
	v_lshrrev_b32_e32 v1, 5, v0
	v_lshrrev_b32_e32 v3, 1, v0
	v_and_b32_e32 v1, 4, v1
	v_bfe_u32 v2, v0, 2, 2
	v_and_b32_e32 v13, 24, v3
	v_or3_b32 v1, v1, v2, v13
	v_lshlrev_b32_e32 v2, 4, v0
	v_or_b32_e32 v10, 0x2000, v2
	s_add_u32 s3, s58, 0x36100000
	v_lshrrev_b32_e32 v3, 7, v10
	s_movk_i32 s6, 0x60
	s_addc_u32 s33, s59, 0
	v_and_or_b32 v4, v3, s6, v1
	v_bfe_u32 v14, v0, 2, 4
	s_movk_i32 s6, 0x70
	s_ashr_i32 s35, s96, 31
	v_and_or_b32 v3, v3, s6, v14
	s_lshr_b32 s6, s35, 29
	s_add_i32 s6, s96, s6
	s_lshr_b32 s12, s7, 6
	s_ashr_i32 s8, s6, 3
	s_and_b32 s6, s6, -8
	s_lshr_b32 s14, s7, 8
	s_lshl_b32 s34, s12, 10
	s_sub_i32 s6, s96, s6
	s_cmp_lt_i32 s6, 0
	s_movk_i32 s36, 0xc1
	s_cselect_b32 s9, s36, 0xc0
	s_mul_i32 s6, s6, s9
	s_add_i32 s6, s6, s8
	s_mul_hi_i32 s8, s6, 0x2aaaaaab
	s_lshr_b32 s9, s8, 31
	s_ashr_i32 s8, s8, 5
	s_add_i32 s8, s8, s9
	s_mul_i32 s9, s8, 0xc0
	s_sub_i32 s9, s6, s9
	s_sext_i32_i16 s6, s9
	s_bfe_u32 s6, s6, 0x3001c
	s_add_i32 s10, s9, s6
	s_sext_i32_i16 s6, s10
	s_and_b32 s10, s10, 0xfff8
	s_sub_i32 s9, s9, s10
	s_lshl_b32 s8, s8, 3
	s_sext_i32_i16 s9, s9
	v_and_b32_e32 v5, 32, v0
	s_lshr_b32 s6, s6, 3
	s_add_i32 s16, s8, s9
	v_bitop3_b32 v11, v2, v5, 48 bitop3:0x6c
	v_and_b32_e32 v12, 64, v0
	s_ashr_i32 s17, s16, 31
	s_bfe_i64 s[10:11], s[6:7], 0x100000
	v_or_b32_e32 v2, v11, v12
	s_lshl_b64 s[8:9], s[16:17], 20
	s_lshl_b64 s[10:11], s[10:11], 20
	v_lshl_or_b32 v132, v3, 12, v2
	v_lshrrev_b32_e32 v3, 3, v0
	s_add_u32 s28, s3, s10
	v_and_or_b32 v1, v3, 32, v1
	s_addc_u32 s29, s33, s11
	s_add_i32 s17, s34, 0
	v_lshl_or_b32 v134, v1, 12, v2
	s_add_i32 m0, s17, 0x10000
	v_lshl_or_b32 v130, v4, 12, v2
	global_load_lds_dwordx4 v134, s[28:29]
	s_add_i32 m0, s17, 0x12000
	s_add_u32 s10, s28, 0x80000
	global_load_lds_dwordx4 v130, s[28:29]
	s_addc_u32 s11, s29, 0
	s_add_i32 m0, s17, 0x14000
	v_and_or_b32 v1, v3, 48, v14
	global_load_lds_dwordx4 v134, s[10:11]
	s_add_i32 m0, s17, 0x16000
	s_add_u32 s26, s82, s8
	s_addc_u32 s27, s83, s9
	s_add_i32 s37, s17, 0x2000
	v_lshl_or_b32 v136, v1, 12, v2
	global_load_lds_dwordx4 v130, s[10:11]
	s_mov_b32 m0, s17
	s_add_u32 s8, s26, 0x80000
	global_load_lds_dwordx4 v136, s[26:27]
	s_mov_b32 m0, s37
	s_addc_u32 s9, s27, 0
	s_add_i32 s38, s17, 0x4000
	global_load_lds_dwordx4 v132, s[26:27]
	s_mov_b32 m0, s38
	s_add_i32 s39, s17, 0x6000
	global_load_lds_dwordx4 v136, s[8:9]
	s_mov_b32 m0, s39
	v_mov_b32_e32 v135, 0
	global_load_lds_dwordx4 v132, s[8:9]
	v_mov_b32_e32 v131, v135
	v_mov_b32_e32 v137, v135
	v_mov_b32_e32 v133, v135
	s_cmp_eq_u32 s14, 1
	s_mov_b32 s40, 0
	v_lshl_add_u64 v[8:9], s[28:29], 0, v[134:135]
	v_lshl_add_u64 v[6:7], s[28:29], 0, v[130:131]
	v_lshl_add_u64 v[2:3], s[26:27], 0, v[136:137]
	s_cselect_b64 s[8:9], -1, 0
	s_cmp_lg_u32 s14, 1
	v_lshl_add_u64 v[4:5], s[26:27], 0, v[132:133]
	s_cbranch_scc1 .LBB0_404
	s_barrier

.LBB0_417:
	s_mov_b32 s2, s101
	s_cmp_gt_i32 s77, 2
	s_cselect_b64 s[6:7], -1, 0
	s_and_b64 s[0:1], s[0:1], s[6:7]
	s_andn2_b64 vcc, exec, s[0:1]
	s_cbranch_vccnz .LBB0_471
	s_waitcnt vmcnt(0)
	s_waitcnt vmcnt(0) lgkmcnt(0)
	s_barrier
	s_mov_b64 s[0:1], exec
	v_readlane_b32 s8, v239, 16
	v_readlane_b32 s9, v239, 17
	s_and_b64 s[8:9], s[0:1], s[8:9]
	s_mov_b64 exec, s[8:9]
	s_cbranch_execz .LBB0_470
	s_add_i32 s3, 0, 0x26020
	v_mov_b32_e32 v1, s3
	s_waitcnt vmcnt(0) expcnt(0) lgkmcnt(0)
	ds_read_b32 v3, v1
	s_add_i32 s3, 0, 0x26024
	v_mov_b32_e32 v1, s3
	ds_read_b32 v1, v1
	s_waitcnt lgkmcnt(1)
	v_cmp_ne_u32_e32 vcc, 0, v3
	s_cbranch_vccnz .LBB0_434
	v_readlane_b32 s8, v239, 34
	v_readlane_b32 s9, v239, 35
	s_load_dwordx2 s[12:13], s[8:9], 0x4
	s_add_u32 s8, s58, 0x1000
	s_addc_u32 s9, s59, 0
	s_add_u32 s10, s58, 0x1100
	s_addc_u32 s11, s59, 0
	s_waitcnt lgkmcnt(0)
	s_mul_i32 s3, s12, s2
	s_add_u32 s12, s58, 0x1200
	s_mul_i32 s3, s3, s13
	s_addc_u32 s13, s59, 0
	s_add_u32 s14, s58, 0x1300
	s_addc_u32 s15, s59, 0
	s_mov_b32 s22, 1
	v_mov_b32_e32 v17, 0
	s_branch .LBB0_422
